# per-unit accumulator zeroing on the matrix pipe (zero-operand i8 MFMAs with C=0, 16 or 4 registers each) instead of 64 packed VALU moves, all five GEMM phases; on top of v80
# speedup vs baseline: 1.0219x; 1.0020x over previous
;     ...
; #pragma unroll
;         for (int a = 0; a < 2; ++a)
; #pragma unroll
;             for (int b = 0; b < 2; ++b)
; #pragma unroll
;                 for (int m = 0; m < 4; ++m)
; #pragma unroll
;                     for (int n = 0; n < 2; ++n) acc[a][b][m][n] = (f32x4){0.f, 0.f, 0.f, 0.f};
.LBB0_487:
	v_mov_b32_e32 v13, v151
	v_mov_b32_e32 v15, v151
	s_add_u32 s3, s6, 0x100
	v_mov_b32_e32 v34, 0
	v_lshl_add_u64 v[16:17], s[20:21], 0, v[14:15]
	v_lshl_add_u64 v[98:99], s[20:21], 0, v[12:13]
	s_addc_u32 s36, s7, 0
	s_mov_b32 s37, -2
	s_mov_b64 s[6:7], 0
	v_pk_mov_b32 v[34:35], 0, 0
	v_pk_mov_b32 v[36:37], 0, 0
	s_nop 1
	v_mfma_i32_16x16x64_i8 v[2:5], v[34:37], v[34:37], 0
	v_mfma_i32_16x16x64_i8 v[6:9], v[34:37], v[34:37], 0
	v_mfma_i32_32x32x32_i8 v[18:33], v[34:37], v[34:37], 0
	v_mfma_i32_32x32x32_i8 v[38:53], v[34:37], v[34:37], 0
	v_mfma_i32_32x32x32_i8 v[54:69], v[34:37], v[34:37], 0
	v_mfma_i32_32x32x32_i8 v[70:85], v[34:37], v[34:37], 0
	v_mfma_i32_16x16x64_i8 v[86:89], v[34:37], v[34:37], 0
	v_mfma_i32_16x16x64_i8 v[90:93], v[34:37], v[34:37], 0
	v_mfma_i32_16x16x64_i8 v[94:97], v[34:37], v[34:37], 0
	v_mfma_i32_16x16x64_i8 v[102:105], v[34:37], v[34:37], 0
	v_mfma_i32_32x32x32_i8 v[110:125], v[34:37], v[34:37], 0
	v_mfma_i32_32x32x32_i8 v[126:141], v[34:37], v[34:37], 0
	v_mfma_i32_16x16x64_i8 v[142:145], v[34:37], v[34:37], 0

;     ...
; #pragma unroll
;         for (int a = 0; a < 2; ++a)
; #pragma unroll
;             for (int b = 0; b < 2; ++b)
; #pragma unroll
;                 for (int m = 0; m < 4; ++m)
; #pragma unroll
;                     for (int n = 0; n < 2; ++n) acc[a][b][m][n] = (f32x4){0.f, 0.f, 0.f, 0.f};
.LBB0_1489:
	v_lshl_or_b32 v184, s50, 8, v198
	v_mov_b32_e32 v179, v173
	v_mov_b32_e32 v181, v173
	s_add_u32 s92, s66, 0x100
	v_mov_b32_e32 v10, 0
	v_lshl_add_u32 v182, s3, 8, v167
	v_ashrrev_i32_e32 v185, 31, v184
	v_lshl_add_u64 v[186:187], s[22:23], 0, v[180:181]
	v_lshl_add_u64 v[188:189], s[22:23], 0, v[178:179]
	s_addc_u32 s93, s67, 0
	s_mov_b32 s94, -2
	s_mov_b64 s[66:67], 0
	v_pk_mov_b32 v[10:11], 0, 0
	v_pk_mov_b32 v[12:13], 0, 0
	s_nop 1
	v_mfma_i32_16x16x64_i8 v[2:5], v[10:13], v[10:13], 0
	v_mfma_i32_16x16x64_i8 v[6:9], v[10:13], v[10:13], 0
	v_mfma_i32_32x32x32_i8 v[14:29], v[10:13], v[10:13], 0
	v_mfma_i32_32x32x32_i8 v[30:45], v[10:13], v[10:13], 0
	v_mfma_i32_32x32x32_i8 v[46:61], v[10:13], v[10:13], 0
	v_mfma_i32_32x32x32_i8 v[62:77], v[10:13], v[10:13], 0
	v_mfma_i32_32x32x32_i8 v[78:93], v[10:13], v[10:13], 0
	v_mfma_i32_32x32x32_i8 v[94:109], v[10:13], v[10:13], 0
	v_mfma_i32_32x32x32_i8 v[110:125], v[10:13], v[10:13], 0
	v_mfma_i32_16x16x64_i8 v[126:129], v[10:13], v[10:13], 0
	s_branch .LBB0_1491

;     ...
; #pragma unroll
;         for (int a = 0; a < 2; ++a)
; #pragma unroll
;             for (int b = 0; b < 2; ++b)
; #pragma unroll
;                 for (int m = 0; m < 4; ++m)
; #pragma unroll
;                     for (int n = 0; n < 2; ++n) acc[a][b][m][n] = (f32x4){0.f, 0.f, 0.f, 0.f};
.LBB0_1652:
	v_mov_b32_e32 v145, v135
	v_mov_b32_e32 v147, v135
	s_add_u32 s80, s62, 0x100
	v_mov_b32_e32 v22, 0
	v_lshl_add_u64 v[148:149], s[24:25], 0, v[146:147]
	v_lshl_add_u64 v[150:151], s[24:25], 0, v[144:145]
	s_addc_u32 s82, s63, 0
	s_mov_b32 s83, -2
	s_mov_b64 s[62:63], 0
	v_pk_mov_b32 v[22:23], 0, 0
	v_pk_mov_b32 v[24:25], 0, 0
	s_nop 1
	v_mfma_i32_32x32x32_i8 v[2:17], v[22:25], v[22:25], 0
	v_mfma_i32_16x16x64_i8 v[18:21], v[22:25], v[22:25], 0
	v_mfma_i32_32x32x32_i8 v[26:41], v[22:25], v[22:25], 0
	v_mfma_i32_32x32x32_i8 v[42:57], v[22:25], v[22:25], 0
	v_mfma_i32_32x32x32_i8 v[58:73], v[22:25], v[22:25], 0
	v_mfma_i32_32x32x32_i8 v[74:89], v[22:25], v[22:25], 0
	v_mfma_i32_32x32x32_i8 v[90:105], v[22:25], v[22:25], 0
	v_mfma_i32_32x32x32_i8 v[106:121], v[22:25], v[22:25], 0
	v_mfma_i32_16x16x64_i8 v[122:125], v[22:25], v[22:25], 0
	v_mfma_i32_16x16x64_i8 v[126:129], v[22:25], v[22:25], 0

;     ...
; #pragma unroll
;         for (int a = 0; a < 2; ++a)
; #pragma unroll
;             for (int b = 0; b < 2; ++b)
; #pragma unroll
;                 for (int m = 0; m < 4; ++m)
; #pragma unroll
;                     for (int n = 0; n < 2; ++n) acc[a][b][m][n] = (f32x4){0.f, 0.f, 0.f, 0.f};
.LBB0_2281:
	s_not_b32 s30, s68
	s_lshl_b32 s30, s30, 10
	s_and_b32 s30, s30, 0x400
	s_add_i32 s30, s30, 0
	s_add_i32 s34, s30, 0x20800
	v_mov_b32_e32 v81, v159
	v_mov_b32_e32 v83, v159
	s_add_u32 s51, s8, 0x100
	v_mov_b32_e32 v30, 0
	v_lshl_add_u64 v[84:85], s[22:23], 0, v[82:83]
	v_lshl_add_u64 v[86:87], s[22:23], 0, v[80:81]
	s_addc_u32 s52, s9, 0
	s_mov_b32 s53, -2
	s_mov_b64 s[30:31], 0
	v_add_u32_e32 v81, s34, v184
	v_add_u32_e32 v83, s34, v185
	v_mov_b32_e32 v189, v79
	v_mov_b32_e32 v191, v78
	v_mov_b32_e32 v190, v80
	v_mov_b32_e32 v192, v82
	v_pk_mov_b32 v[30:31], 0, 0
	v_pk_mov_b32 v[32:33], 0, 0
	s_nop 1
	v_mfma_i32_32x32x32_i8 v[2:17], v[30:33], v[30:33], 0
	v_mfma_i32_16x16x64_i8 v[18:21], v[30:33], v[30:33], 0
	v_mfma_i32_16x16x64_i8 v[22:25], v[30:33], v[30:33], 0
	v_mfma_i32_16x16x64_i8 v[26:29], v[30:33], v[30:33], 0
	v_mfma_i32_32x32x32_i8 v[34:49], v[30:33], v[30:33], 0
	v_mfma_i32_32x32x32_i8 v[50:65], v[30:33], v[30:33], 0
	v_mfma_i32_16x16x64_i8 v[66:69], v[30:33], v[30:33], 0
	v_mfma_i32_16x16x64_i8 v[70:73], v[30:33], v[30:33], 0
	v_mfma_i32_16x16x64_i8 v[74:77], v[30:33], v[30:33], 0
	v_mfma_i32_16x16x64_i8 v[90:93], v[30:33], v[30:33], 0
	v_mfma_i32_16x16x64_i8 v[94:97], v[30:33], v[30:33], 0
	v_mfma_i32_32x32x32_i8 v[110:125], v[30:33], v[30:33], 0
	v_mfma_i32_32x32x32_i8 v[126:141], v[30:33], v[30:33], 0
	v_mfma_i32_16x16x64_i8 v[142:145], v[30:33], v[30:33], 0
	v_mfma_i32_16x16x64_i8 v[146:149], v[30:33], v[30:33], 0
	v_mfma_i32_16x16x64_i8 v[150:153], v[30:33], v[30:33], 0
	s_branch .LBB0_2283

;     ...
; #pragma unroll
;         for (int a = 0; a < 2; ++a)
; #pragma unroll
;             for (int b = 0; b < 2; ++b)
; #pragma unroll
;                 for (int m = 0; m < 4; ++m)
; #pragma unroll
;                     for (int n = 0; n < 2; ++n) acc[a][b][m][n] = (f32x4){0.f, 0.f, 0.f, 0.f};
.LBB0_2450:
	v_mov_b32_e32 v119, v157
	v_mov_b32_e32 v125, v157
	s_add_u32 s50, s38, 0x100
	v_mov_b32_e32 v24, 0
	v_lshl_add_u64 v[126:127], s[30:31], 0, v[124:125]
	v_lshl_add_u64 v[136:137], s[30:31], 0, v[118:119]
	s_addc_u32 s51, s39, 0
	s_mov_b32 s52, -2
	s_mov_b64 s[38:39], 0
	v_pk_mov_b32 v[24:25], 0, 0
	v_pk_mov_b32 v[26:27], 0, 0
	s_nop 1
	v_mfma_i32_32x32x32_i8 v[0:15], v[24:27], v[24:27], 0
	v_mfma_i32_16x16x64_i8 v[16:19], v[24:27], v[24:27], 0
	v_mfma_i32_16x16x64_i8 v[20:23], v[24:27], v[24:27], 0
	v_mfma_i32_32x32x32_i8 v[28:43], v[24:27], v[24:27], 0
	v_mfma_i32_32x32x32_i8 v[44:59], v[24:27], v[24:27], 0
	v_mfma_i32_32x32x32_i8 v[60:75], v[24:27], v[24:27], 0
	v_mfma_i32_32x32x32_i8 v[76:91], v[24:27], v[24:27], 0
	v_mfma_i32_32x32x32_i8 v[92:107], v[24:27], v[24:27], 0
	v_mfma_i32_16x16x64_i8 v[108:111], v[24:27], v[24:27], 0
	v_mfma_i32_16x16x64_i8 v[112:115], v[24:27], v[24:27], 0
	v_mfma_i32_16x16x64_i8 v[120:123], v[24:27], v[24:27], 0
	v_mfma_i32_16x16x64_i8 v[128:131], v[24:27], v[24:27], 0
	v_mfma_i32_16x16x64_i8 v[132:135], v[24:27], v[24:27], 0
